# speedup vs baseline: 1.0256x; 1.0017x over previous
_Z5k_decPKiPKDF16_S2_PKfS4_S4_Pf:
	s_load_dword s3, s[0:1], 0x44
	s_load_dword s6, s[0:1], 0x38
	s_load_dwordx2 s[4:5], s[0:1], 0x0
	s_load_dwordx8 s[28:35], s[0:1], 0x8
	s_load_dwordx4 s[12:15], s[0:1], 0x28
	v_and_b32_e32 v1, 15, v0
	v_and_b32_e32 v64, 63, v0
	v_lshlrev_b32_e32 v96, 3, v1
	v_lshrrev_b32_e32 v4, 3, v0
	v_and_b32_e32 v4, 4, v4
	v_or_b32_e32 v96, v96, v4
	v_mov_b32_e32 v97, 0
	v_and_b32_e32 v104, 16, v0
	v_lshlrev_b32_e32 v6, 7, v0
	v_lshlrev_b32_e32 v7, 2, v64
	s_movk_i32 s16, 0x6000
	v_and_or_b32 v103, v6, s16, v7
	v_mov_b32_e32 v219, 0
	s_movk_i32 s19, 0x3d08
	s_waitcnt lgkmcnt(0)
	s_and_b32 s3, s3, 0xffff
	s_mul_i32 s2, s2, s3
	v_add_u32_e32 v5, s2, v0
	s_mul_i32 s6, s6, s3
	v_lshrrev_b32_e32 v102, 6, v5
	s_lshr_b32 s18, s6, 6
	v_readfirstlane_b32 s23, v102
	v_lshl_add_u64 v[2:3], s[4:5], 0, v[96:97]
	s_mov_b32 s16, 0xf4240
	v_cmp_gt_u32_e32 vcc, s16, v5
	s_and_saveexec_b64 s[22:23], vcc
	s_cbranch_execz .LBB2_3
	v_mov_b32_e32 v222, v2
	v_mov_b32_e32 v223, v3
	v_min_u32_e32 v218, s19, v102
	v_lshlrev_b32_e32 v218, 9, v218
	v_lshl_add_u64 v[216:217], v[222:223], 0, v[218:219]
	global_load_dword v65, v[216:217], off nt
	global_load_dword v80, v[216:217], off offset:128 nt
	global_load_dword v81, v[216:217], off offset:256 nt
	global_load_dword v82, v[216:217], off offset:384 nt
	v_add_u32_e32 v220, s18, v102
	v_min_u32_e32 v218, s19, v220
	v_lshlrev_b32_e32 v218, 9, v218
	v_lshl_add_u64 v[216:217], v[222:223], 0, v[218:219]
	global_load_dword v100, v[216:217], off nt
	global_load_dword v101, v[216:217], off offset:128 nt
	global_load_dword v98, v[216:217], off offset:256 nt
	global_load_dword v99, v[216:217], off offset:384 nt
	s_mov_b32 s8, s28
	s_and_b32 s9, s29, 0xffff
	s_mov_b32 s10, 0x30d400
	s_mov_b32 s11, 0x20000
	s_mov_b64 s[36:37], 0x1000
	v_and_b32_e32 v96, 48, v64
	v_lshlrev_b32_e32 v221, 6, v1
	v_lshlrev_b32_e32 v211, 2, v1
	v_lshlrev_b32_e32 v214, 4, v0
	v_add_u32_e32 v215, 0x1000, v214
	v_lshl_add_u32 v134, v1, 6, v96
	v_add_u32_e32 v134, 0x9000, v134
	v_add_u32_e32 v133, 0x9000, v214
	v_lshl_or_b32 v221, v102, 6, v64
	v_lshrrev_b32_e32 v213, 4, v64
	v_cmp_gt_u32_e32 vcc, 16, v64
	v_and_b32_e32 v210, 31, v64
	v_lshlrev_b32_e32 v210, 4, v210
	s_mov_b32 s38, -1
	s_mov_b32 s39, 0
	s_mov_b64 exec, s[38:39]
	global_load_dwordx4 v[126:129], v210, s[32:33]
	s_mov_b32 s38, 0
	s_mov_b32 s39, -1
	s_mov_b64 exec, s[38:39]
	global_load_dwordx4 v[126:129], v210, s[34:35]
	s_mov_b64 exec, -1
	global_load_dwordx4 v[32:35], v214, s[30:31]
	global_load_dwordx4 v[36:39], v215, s[30:31]
	s_load_dword s12, s[12:13], 0x0
	s_waitcnt vmcnt(8)
	v_lshl_or_b32 v216, v65, 5, v104
	v_lshl_or_b32 v217, v80, 5, v104
	v_lshl_or_b32 v218, v81, 5, v104
	v_lshl_or_b32 v212, v82, 5, v104
	buffer_load_dwordx4 v[92:95], v216, s[8:11], 0 offen
	buffer_load_dwordx4 v[88:91], v217, s[8:11], 0 offen
	buffer_load_dwordx4 v[84:87], v218, s[8:11], 0 offen
	buffer_load_dwordx4 v[80:83], v212, s[8:11], 0 offen
	s_lshl_b32 s21, s18, 6
	s_mov_b32 s20, 2
	s_mov_b64 s[16:17], 0
	v_cmp_eq_u32_e64 s[0:1], 1, v213
	v_cmp_eq_u32_e64 s[2:3], 2, v213
	v_cmp_eq_u32_e64 s[4:5], 3, v213
	v_mov_b32_e32 v96, v221
	v_mov_b32_e32 v97, 0
	s_waitcnt vmcnt(4)
	v_lshrrev_b32_e32 v210, 6, v0
	v_lshlrev_b32_e32 v210, 10, v210
	v_add_u32_e32 v210, 0x8000, v210
	v_lshl_add_u32 v130, v64, 4, v210
	v_lshl_add_u32 v131, v213, 4, v210
	v_add_u32_e32 v132, v211, v210
	ds_write_b128 v130, v[126:129]
	ds_write_b128 v133, v[32:35]
	ds_write_b128 v133, v[36:39] offset:4096
	ds_read_b128 v[68:71], v131 offset:512
	ds_read_b128 v[72:75], v131 offset:576
	ds_read_b128 v[76:79], v131 offset:640
	ds_read_b128 v[106:109], v131 offset:704
	ds_read_b128 v[110:113], v131 offset:768
	ds_read_b128 v[114:117], v131 offset:832
	ds_read_b128 v[118:121], v131 offset:896
	ds_read_b128 v[122:125], v131 offset:960
	s_waitcnt lgkmcnt(0)
	ds_read_b32 v148, v132 offset:512
	ds_read_b32 v149, v132 offset:576
	ds_read_b32 v150, v132 offset:640
	ds_read_b32 v151, v132 offset:704
	ds_read_b32 v152, v132 offset:768
	ds_read_b32 v153, v132 offset:832
	ds_read_b32 v154, v132 offset:896
	ds_read_b32 v155, v132 offset:960
	ds_read_b32 v156, v132 offset:0
	ds_read_b32 v157, v132 offset:64
	ds_read_b32 v158, v132 offset:128
	ds_read_b32 v159, v132 offset:192
	s_waitcnt lgkmcnt(0)
	ds_read_b32 v160, v132 offset:256
	ds_read_b32 v161, v132 offset:320
	ds_read_b32 v162, v132 offset:384
	ds_read_b32 v163, v132 offset:448
	ds_read_b128 v[0:3], v131 offset:0
	ds_read_b128 v[4:7], v131 offset:64
	ds_read_b128 v[8:11], v131 offset:128
	ds_read_b128 v[12:15], v131 offset:192
	ds_read_b128 v[16:19], v131 offset:256
	ds_read_b128 v[20:23], v131 offset:320
	ds_read_b128 v[24:27], v131 offset:384
	ds_read_b128 v[28:31], v131 offset:448
	s_waitcnt lgkmcnt(0)
	s_barrier
	ds_read_b128 v[32:35], v134
	ds_read_b128 v[36:39], v134 offset:1024
	ds_read_b128 v[40:43], v134 offset:2048
	ds_read_b128 v[44:47], v134 offset:3072
	ds_read_b128 v[48:51], v134 offset:4096
	ds_read_b128 v[52:55], v134 offset:5120
	ds_read_b128 v[56:59], v134 offset:6144
	ds_read_b128 v[60:63], v134 offset:7168
	v_cvt_pk_f16_f32 v67, v74, v75
	v_cvt_pk_f16_f32 v66, v72, v73
	v_cvt_pk_f16_f32 v65, v70, v71
	v_cvt_pk_f16_f32 v64, v68, v69
	v_cvt_pk_f16_f32 v71, v108, v109
	v_cvt_pk_f16_f32 v70, v106, v107
	v_cvt_pk_f16_f32 v69, v78, v79
	v_cvt_pk_f16_f32 v68, v76, v77
	v_cvt_pk_f16_f32 v75, v116, v117
	v_cvt_pk_f16_f32 v74, v114, v115
	v_cvt_pk_f16_f32 v73, v112, v113
	v_cvt_pk_f16_f32 v72, v110, v111
	v_cvt_pk_f16_f32 v79, v124, v125
	v_cvt_pk_f16_f32 v78, v122, v123
	v_cvt_pk_f16_f32 v77, v120, v121
	v_cvt_pk_f16_f32 v76, v118, v119
	v_mov_b32_e32 v167, 0x38003800
	v_pk_mul_f16 v64, v64, v167
	v_pk_mul_f16 v65, v65, v167
	v_pk_mul_f16 v66, v66, v167
	v_pk_mul_f16 v67, v67, v167
	v_pk_mul_f16 v68, v68, v167
	v_pk_mul_f16 v69, v69, v167
	v_pk_mul_f16 v70, v70, v167
	v_pk_mul_f16 v71, v71, v167
	v_pk_mul_f16 v72, v72, v167
	v_pk_mul_f16 v73, v73, v167
	v_pk_mul_f16 v74, v74, v167
	v_pk_mul_f16 v75, v75, v167
	v_pk_mul_f16 v76, v76, v167
	v_pk_mul_f16 v77, v77, v167
	v_pk_mul_f16 v78, v78, v167
	v_pk_mul_f16 v79, v79, v167
	v_cvt_f16_f32_e32 v148, v148
	v_cvt_f16_f32_e32 v149, v149
	v_cvt_f16_f32_e32 v150, v150
	v_cvt_f16_f32_e32 v151, v151
	v_cvt_f16_f32_e32 v152, v152
	v_cvt_f16_f32_e32 v153, v153
	v_cvt_f16_f32_e32 v154, v154
	v_cvt_f16_f32_e32 v155, v155
	v_cvt_f32_f16_e32 v148, v148
	v_cvt_f32_f16_e32 v149, v149
	v_cvt_f32_f16_e32 v150, v150
	v_cvt_f32_f16_e32 v151, v151
	v_cvt_f32_f16_e32 v152, v152
	v_cvt_f32_f16_e32 v153, v153
	v_cvt_f32_f16_e32 v154, v154
	v_cvt_f32_f16_e32 v155, v155
	v_mul_f32_e32 v148, 0.5, v148
	v_mul_f32_e32 v149, 0.5, v149
	v_mul_f32_e32 v150, 0.5, v150
	v_mul_f32_e32 v151, 0.5, v151
	v_mul_f32_e32 v152, 0.5, v152
	v_mul_f32_e32 v153, 0.5, v153
	v_mul_f32_e32 v154, 0.5, v154
	v_mul_f32_e32 v155, 0.5, v155
	v_mov_b32_e32 v140, 0
	v_mov_b32_e32 v141, 0
	v_mov_b32_e32 v142, 0
	v_mov_b32_e32 v143, 0
	v_mov_b32_e32 v144, 0
	v_mov_b32_e32 v145, 0
	v_mov_b32_e32 v146, 0
	v_mov_b32_e32 v147, 0
	v_mov_b32_e32 v166, 0
	s_waitcnt lgkmcnt(0)
	v_cvt_f32_f16_e32 v164, v32
	v_cvt_f32_f16_sdwa v165, v32 dst_sel:DWORD dst_unused:UNUSED_PAD src0_sel:WORD_1
	v_fmac_f32_e32 v140, v148, v164
	v_fmac_f32_e32 v141, v148, v165
	v_cvt_f32_f16_e32 v164, v33
	v_cvt_f32_f16_sdwa v165, v33 dst_sel:DWORD dst_unused:UNUSED_PAD src0_sel:WORD_1
	v_fmac_f32_e32 v142, v148, v164
	v_fmac_f32_e32 v143, v148, v165
	v_cvt_f32_f16_e32 v164, v34
	v_cvt_f32_f16_sdwa v165, v34 dst_sel:DWORD dst_unused:UNUSED_PAD src0_sel:WORD_1
	v_fmac_f32_e32 v144, v148, v164
	v_fmac_f32_e32 v145, v148, v165
	v_cvt_f32_f16_e32 v164, v35
	v_cvt_f32_f16_sdwa v165, v35 dst_sel:DWORD dst_unused:UNUSED_PAD src0_sel:WORD_1
	v_fmac_f32_e32 v146, v148, v164
	v_fmac_f32_e32 v147, v148, v165
	v_fmac_f32_e32 v166, v148, v156
	v_cvt_f32_f16_e32 v164, v36
	v_cvt_f32_f16_sdwa v165, v36 dst_sel:DWORD dst_unused:UNUSED_PAD src0_sel:WORD_1
	v_fmac_f32_e32 v140, v149, v164
	v_fmac_f32_e32 v141, v149, v165
	v_cvt_f32_f16_e32 v164, v37
	v_cvt_f32_f16_sdwa v165, v37 dst_sel:DWORD dst_unused:UNUSED_PAD src0_sel:WORD_1
	v_fmac_f32_e32 v142, v149, v164
	v_fmac_f32_e32 v143, v149, v165
	v_cvt_f32_f16_e32 v164, v38
	v_cvt_f32_f16_sdwa v165, v38 dst_sel:DWORD dst_unused:UNUSED_PAD src0_sel:WORD_1
	v_fmac_f32_e32 v144, v149, v164
	v_fmac_f32_e32 v145, v149, v165
	v_cvt_f32_f16_e32 v164, v39
	v_cvt_f32_f16_sdwa v165, v39 dst_sel:DWORD dst_unused:UNUSED_PAD src0_sel:WORD_1
	v_fmac_f32_e32 v146, v149, v164
	v_fmac_f32_e32 v147, v149, v165
	v_fmac_f32_e32 v166, v149, v157
	v_cvt_f32_f16_e32 v164, v40
	v_cvt_f32_f16_sdwa v165, v40 dst_sel:DWORD dst_unused:UNUSED_PAD src0_sel:WORD_1
	v_fmac_f32_e32 v140, v150, v164
	v_fmac_f32_e32 v141, v150, v165
	v_cvt_f32_f16_e32 v164, v41
	v_cvt_f32_f16_sdwa v165, v41 dst_sel:DWORD dst_unused:UNUSED_PAD src0_sel:WORD_1
	v_fmac_f32_e32 v142, v150, v164
	v_fmac_f32_e32 v143, v150, v165
	v_cvt_f32_f16_e32 v164, v42
	v_cvt_f32_f16_sdwa v165, v42 dst_sel:DWORD dst_unused:UNUSED_PAD src0_sel:WORD_1
	v_fmac_f32_e32 v144, v150, v164
	v_fmac_f32_e32 v145, v150, v165
	v_cvt_f32_f16_e32 v164, v43
	v_cvt_f32_f16_sdwa v165, v43 dst_sel:DWORD dst_unused:UNUSED_PAD src0_sel:WORD_1
	v_fmac_f32_e32 v146, v150, v164
	v_fmac_f32_e32 v147, v150, v165
	v_fmac_f32_e32 v166, v150, v158
	v_cvt_f32_f16_e32 v164, v44
	v_cvt_f32_f16_sdwa v165, v44 dst_sel:DWORD dst_unused:UNUSED_PAD src0_sel:WORD_1
	v_fmac_f32_e32 v140, v151, v164
	v_fmac_f32_e32 v141, v151, v165
	v_cvt_f32_f16_e32 v164, v45
	v_cvt_f32_f16_sdwa v165, v45 dst_sel:DWORD dst_unused:UNUSED_PAD src0_sel:WORD_1
	v_fmac_f32_e32 v142, v151, v164
	v_fmac_f32_e32 v143, v151, v165
	v_cvt_f32_f16_e32 v164, v46
	v_cvt_f32_f16_sdwa v165, v46 dst_sel:DWORD dst_unused:UNUSED_PAD src0_sel:WORD_1
	v_fmac_f32_e32 v144, v151, v164
	v_fmac_f32_e32 v145, v151, v165
	v_cvt_f32_f16_e32 v164, v47
	v_cvt_f32_f16_sdwa v165, v47 dst_sel:DWORD dst_unused:UNUSED_PAD src0_sel:WORD_1
	v_fmac_f32_e32 v146, v151, v164
	v_fmac_f32_e32 v147, v151, v165
	v_fmac_f32_e32 v166, v151, v159
	v_cvt_f32_f16_e32 v164, v48
	v_cvt_f32_f16_sdwa v165, v48 dst_sel:DWORD dst_unused:UNUSED_PAD src0_sel:WORD_1
	v_fmac_f32_e32 v140, v152, v164
	v_fmac_f32_e32 v141, v152, v165
	v_cvt_f32_f16_e32 v164, v49
	v_cvt_f32_f16_sdwa v165, v49 dst_sel:DWORD dst_unused:UNUSED_PAD src0_sel:WORD_1
	v_fmac_f32_e32 v142, v152, v164
	v_fmac_f32_e32 v143, v152, v165
	v_cvt_f32_f16_e32 v164, v50
	v_cvt_f32_f16_sdwa v165, v50 dst_sel:DWORD dst_unused:UNUSED_PAD src0_sel:WORD_1
	v_fmac_f32_e32 v144, v152, v164
	v_fmac_f32_e32 v145, v152, v165
	v_cvt_f32_f16_e32 v164, v51
	v_cvt_f32_f16_sdwa v165, v51 dst_sel:DWORD dst_unused:UNUSED_PAD src0_sel:WORD_1
	v_fmac_f32_e32 v146, v152, v164
	v_fmac_f32_e32 v147, v152, v165
	v_fmac_f32_e32 v166, v152, v160
	v_cvt_f32_f16_e32 v164, v52
	v_cvt_f32_f16_sdwa v165, v52 dst_sel:DWORD dst_unused:UNUSED_PAD src0_sel:WORD_1
	v_fmac_f32_e32 v140, v153, v164
	v_fmac_f32_e32 v141, v153, v165
	v_cvt_f32_f16_e32 v164, v53
	v_cvt_f32_f16_sdwa v165, v53 dst_sel:DWORD dst_unused:UNUSED_PAD src0_sel:WORD_1
	v_fmac_f32_e32 v142, v153, v164
	v_fmac_f32_e32 v143, v153, v165
	v_cvt_f32_f16_e32 v164, v54
	v_cvt_f32_f16_sdwa v165, v54 dst_sel:DWORD dst_unused:UNUSED_PAD src0_sel:WORD_1
	v_fmac_f32_e32 v144, v153, v164
	v_fmac_f32_e32 v145, v153, v165
	v_cvt_f32_f16_e32 v164, v55
	v_cvt_f32_f16_sdwa v165, v55 dst_sel:DWORD dst_unused:UNUSED_PAD src0_sel:WORD_1
	v_fmac_f32_e32 v146, v153, v164
	v_fmac_f32_e32 v147, v153, v165
	v_fmac_f32_e32 v166, v153, v161
	v_cvt_f32_f16_e32 v164, v56
	v_cvt_f32_f16_sdwa v165, v56 dst_sel:DWORD dst_unused:UNUSED_PAD src0_sel:WORD_1
	v_fmac_f32_e32 v140, v154, v164
	v_fmac_f32_e32 v141, v154, v165
	v_cvt_f32_f16_e32 v164, v57
	v_cvt_f32_f16_sdwa v165, v57 dst_sel:DWORD dst_unused:UNUSED_PAD src0_sel:WORD_1
	v_fmac_f32_e32 v142, v154, v164
	v_fmac_f32_e32 v143, v154, v165
	v_cvt_f32_f16_e32 v164, v58
	v_cvt_f32_f16_sdwa v165, v58 dst_sel:DWORD dst_unused:UNUSED_PAD src0_sel:WORD_1
	v_fmac_f32_e32 v144, v154, v164
	v_fmac_f32_e32 v145, v154, v165
	v_cvt_f32_f16_e32 v164, v59
	v_cvt_f32_f16_sdwa v165, v59 dst_sel:DWORD dst_unused:UNUSED_PAD src0_sel:WORD_1
	v_fmac_f32_e32 v146, v154, v164
	v_fmac_f32_e32 v147, v154, v165
	v_fmac_f32_e32 v166, v154, v162
	v_cvt_f32_f16_e32 v164, v60
	v_cvt_f32_f16_sdwa v165, v60 dst_sel:DWORD dst_unused:UNUSED_PAD src0_sel:WORD_1
	v_fmac_f32_e32 v140, v155, v164
	v_fmac_f32_e32 v141, v155, v165
	v_cvt_f32_f16_e32 v164, v61
	v_cvt_f32_f16_sdwa v165, v61 dst_sel:DWORD dst_unused:UNUSED_PAD src0_sel:WORD_1
	v_fmac_f32_e32 v142, v155, v164
	v_fmac_f32_e32 v143, v155, v165
	v_cvt_f32_f16_e32 v164, v62
	v_cvt_f32_f16_sdwa v165, v62 dst_sel:DWORD dst_unused:UNUSED_PAD src0_sel:WORD_1
	v_fmac_f32_e32 v144, v155, v164
	v_fmac_f32_e32 v145, v155, v165
	v_cvt_f32_f16_e32 v164, v63
	v_cvt_f32_f16_sdwa v165, v63 dst_sel:DWORD dst_unused:UNUSED_PAD src0_sel:WORD_1
	v_fmac_f32_e32 v146, v155, v164
	v_fmac_f32_e32 v147, v155, v165
	v_fmac_f32_e32 v166, v155, v163
	v_add_f32_dpp v140, v140, v140 row_ror:8 row_mask:0xf bank_mask:0xf
	v_add_f32_dpp v141, v141, v141 row_ror:8 row_mask:0xf bank_mask:0xf
	v_add_f32_dpp v142, v142, v142 row_ror:8 row_mask:0xf bank_mask:0xf
	v_add_f32_dpp v143, v143, v143 row_ror:8 row_mask:0xf bank_mask:0xf
	v_add_f32_dpp v144, v144, v144 row_ror:8 row_mask:0xf bank_mask:0xf
	v_add_f32_dpp v145, v145, v145 row_ror:8 row_mask:0xf bank_mask:0xf
	v_add_f32_dpp v146, v146, v146 row_ror:8 row_mask:0xf bank_mask:0xf
	v_add_f32_dpp v147, v147, v147 row_ror:8 row_mask:0xf bank_mask:0xf
	v_add_f32_dpp v166, v166, v166 row_ror:8 row_mask:0xf bank_mask:0xf
	v_add_f32_dpp v140, v140, v140 row_ror:4 row_mask:0xf bank_mask:0xf
	v_add_f32_dpp v141, v141, v141 row_ror:4 row_mask:0xf bank_mask:0xf
	v_add_f32_dpp v142, v142, v142 row_ror:4 row_mask:0xf bank_mask:0xf
	v_add_f32_dpp v143, v143, v143 row_ror:4 row_mask:0xf bank_mask:0xf
	v_add_f32_dpp v144, v144, v144 row_ror:4 row_mask:0xf bank_mask:0xf
	v_add_f32_dpp v145, v145, v145 row_ror:4 row_mask:0xf bank_mask:0xf
	v_add_f32_dpp v146, v146, v146 row_ror:4 row_mask:0xf bank_mask:0xf
	v_add_f32_dpp v147, v147, v147 row_ror:4 row_mask:0xf bank_mask:0xf
	v_add_f32_dpp v166, v166, v166 row_ror:4 row_mask:0xf bank_mask:0xf
	v_add_f32_dpp v140, v140, v140 row_ror:2 row_mask:0xf bank_mask:0xf
	v_add_f32_dpp v141, v141, v141 row_ror:2 row_mask:0xf bank_mask:0xf
	v_add_f32_dpp v142, v142, v142 row_ror:2 row_mask:0xf bank_mask:0xf
	v_add_f32_dpp v143, v143, v143 row_ror:2 row_mask:0xf bank_mask:0xf
	v_add_f32_dpp v144, v144, v144 row_ror:2 row_mask:0xf bank_mask:0xf
	v_add_f32_dpp v145, v145, v145 row_ror:2 row_mask:0xf bank_mask:0xf
	v_add_f32_dpp v146, v146, v146 row_ror:2 row_mask:0xf bank_mask:0xf
	v_add_f32_dpp v147, v147, v147 row_ror:2 row_mask:0xf bank_mask:0xf
	v_add_f32_dpp v166, v166, v166 row_ror:2 row_mask:0xf bank_mask:0xf
	v_add_f32_dpp v140, v140, v140 row_ror:1 row_mask:0xf bank_mask:0xf
	v_add_f32_dpp v141, v141, v141 row_ror:1 row_mask:0xf bank_mask:0xf
	v_add_f32_dpp v142, v142, v142 row_ror:1 row_mask:0xf bank_mask:0xf
	v_add_f32_dpp v143, v143, v143 row_ror:1 row_mask:0xf bank_mask:0xf
	v_add_f32_dpp v144, v144, v144 row_ror:1 row_mask:0xf bank_mask:0xf
	v_add_f32_dpp v145, v145, v145 row_ror:1 row_mask:0xf bank_mask:0xf
	v_add_f32_dpp v146, v146, v146 row_ror:1 row_mask:0xf bank_mask:0xf
	v_add_f32_dpp v147, v147, v147 row_ror:1 row_mask:0xf bank_mask:0xf
	v_add_f32_dpp v166, v166, v166 row_ror:1 row_mask:0xf bank_mask:0xf
	v_cvt_pk_f16_f32 v252, v140, v141
	v_cvt_pk_f16_f32 v253, v142, v143
	v_cvt_pk_f16_f32 v254, v144, v145
	v_cvt_pk_f16_f32 v255, v146, v147
	s_waitcnt lgkmcnt(0)
	v_add_f32_e32 v209, s12, v166
	v_add_u32_e32 v220, s18, v102
	v_add_u32_e32 v220, s18, v220
	v_min_u32_e32 v218, s19, v220
	v_lshlrev_b32_e32 v218, 9, v218
	v_lshl_add_u64 v[216:217], v[222:223], 0, v[218:219]
	global_load_dword v228, v[216:217], off nt
	global_load_dword v229, v[216:217], off offset:128 nt
	global_load_dword v230, v[216:217], off offset:256 nt
	global_load_dword v231, v[216:217], off offset:384 nt
	v_add_u32_e32 v220, s18, v220
	v_min_u32_e32 v218, s19, v220
	v_lshlrev_b32_e32 v218, 9, v218
	v_lshl_add_u64 v[216:217], v[222:223], 0, v[218:219]
	global_load_dword v232, v[216:217], off nt
	global_load_dword v233, v[216:217], off offset:128 nt
	global_load_dword v234, v[216:217], off offset:256 nt
	global_load_dword v235, v[216:217], off offset:384 nt
	v_add_u32_e32 v220, s18, v220
	v_min_u32_e32 v218, s19, v220
	v_lshlrev_b32_e32 v218, 9, v218
	v_lshl_add_u64 v[216:217], v[222:223], 0, v[218:219]
	global_load_dword v236, v[216:217], off nt
	global_load_dword v237, v[216:217], off offset:128 nt
	global_load_dword v238, v[216:217], off offset:256 nt
	global_load_dword v239, v[216:217], off offset:384 nt
	v_add_u32_e32 v220, s18, v220
	v_min_u32_e32 v218, s19, v220
	v_lshlrev_b32_e32 v218, 9, v218
	v_lshl_add_u64 v[216:217], v[222:223], 0, v[218:219]
	global_load_dword v240, v[216:217], off nt
	global_load_dword v241, v[216:217], off offset:128 nt
	global_load_dword v242, v[216:217], off offset:256 nt
	global_load_dword v243, v[216:217], off offset:384 nt
	v_add_u32_e32 v220, s18, v220
	v_min_u32_e32 v218, s19, v220
	v_lshlrev_b32_e32 v218, 9, v218
	v_lshl_add_u64 v[216:217], v[222:223], 0, v[218:219]
	global_load_dword v244, v[216:217], off nt
	global_load_dword v245, v[216:217], off offset:128 nt
	global_load_dword v246, v[216:217], off offset:256 nt
	global_load_dword v247, v[216:217], off offset:384 nt
	v_add_u32_e32 v220, s18, v220
	v_min_u32_e32 v218, s19, v220
	v_lshlrev_b32_e32 v218, 9, v218
	v_lshl_add_u64 v[216:217], v[222:223], 0, v[218:219]
	global_load_dword v248, v[216:217], off nt
	global_load_dword v249, v[216:217], off offset:128 nt
	global_load_dword v250, v[216:217], off offset:256 nt
	global_load_dword v251, v[216:217], off offset:384 nt
	s_waitcnt vmcnt(24)
